# conversion order reversed (W_down items first in P2, gate/up last in P5) so P9 finds the most recently converted weights closer; on top of v113
# baseline (speedup 1.0000x reference)
; #define SEAM(k) do { if (IN(k) && IN((k) + 1)) xcd_barrier(bar); } while (0)
; #define REP(k) for (int _rep = 0; _rep < ((PROBE_DBL == (k)) ? 2 : 1); ++_rep)
; __device__ __forceinline__ void convert_load(Frame& F, int it, f32x4 (&v)[16]) {
;     const int mat = it / TI_PER_MAT, r = it % TI_PER_MAT, type = mat / NE, e = mat % NE, kb = r >> 3, n4 = (r & 7) * 256 + F.lane * 4;
;     const float* src = F.in[type == 0 ? I_WGATE : (type == 1 ? I_WUP : I_WDOWN)] + (size_t)e * D * D + (size_t)(kb * 16) * D + n4;
; #pragma unroll
;     for (int i = 0; i < 16; ++i) v[i] = __builtin_nontemporal_load((const f32x4*)(src + (size_t)i * D));
; }
; __device__ __forceinline__ void convert_store(Frame& F, int it, const f32x4 (&v)[16]) {
;     const int mat = it / TI_PER_MAT, r = it % TI_PER_MAT, type = mat / NE, e = mat % NE, kb = r >> 3, n4 = (r & 7) * 256 + F.lane * 4;
;     unsigned char* dst = F.ws + (type == 0 ? WS_WG : (type == 1 ? WS_WU : WS_WD)) + (size_t)e * D * D + ((size_t)kb * D + n4) * 16;
; #pragma unroll
;     for (int nn = 0; nn < 4; ++nn)
;         *(u32x4*)(dst + nn * 16) = (u32x4){pk_fp8x4(v[0][nn] * W8_SCALE, v[1][nn] * W8_SCALE, v[2][nn] * W8_SCALE, v[3][nn] * W8_SCALE), pk_fp8x4(v[4][nn] * W8_SCALE, v[5][nn] * W8_SCALE, v[6][nn] * W8_SCALE, v[7][nn] * W8_SCALE),
;                                           pk_fp8x4(v[8][nn] * W8_SCALE, v[9][nn] * W8_SCALE, v[10][nn] * W8_SCALE, v[11][nn] * W8_SCALE), pk_fp8x4(v[12][nn] * W8_SCALE, v[13][nn] * W8_SCALE, v[14][nn] * W8_SCALE, v[15][nn] * W8_SCALE)};
; }
; __device__ __forceinline__ void convert_experts(Frame& F, int gw, int NGW, int it0, int it1) {
;     f32x4 A[16], B[16];
;     for (int it = it0 + gw; it < it1; it += 2 * NGW) {
;         const int i2 = it + NGW; const bool h2 = i2 < it1;
;         convert_load(F, it, A); convert_load(F, h2 ? i2 : it, B); __builtin_amdgcn_sched_barrier(0);
; __global__ void __launch_bounds__(512, 2) fwd_kernel(Args args) {
;     ...
;     if (IN(2)) REP(2) { const int gconv = (F.G > 2 * NCONV_WG) ? NCONV_WG : 0, ggemm = F.G - gconv;
;                  if (F.bid < ggemm) { InProj S{D, (const char*)WSP(bf16_t, WS_HM), (const char*)WSP(bf16_t, WS_WIN), WSP(bf16_t, WS_P), ggemm, F.bid}; pg8::gemm_phase(F.lds, S); }
;                  else if (PROBE_DBL != 2 || _rep == 0) convert_experts(F, (F.bid - ggemm) * 8 + F.wave, gconv * 8, 0, ti_early(F.G)); } SEAM(2);
.LBB0_199:
	s_cmp_lt_i32 s68, 3
	s_cselect_b64 s[0:1], -1, 0
	s_and_b64 s[2:3], s[0:1], s[4:5]
	s_andn2_b64 vcc, exec, s[2:3]
	s_cbranch_vccnz .LBB0_227
	s_cmp_gt_i32 s79, 40
	s_cselect_b64 s[2:3], -1, 0
	s_and_b64 s[4:5], s[2:3], exec
	s_cselect_b32 s6, 20, 0
	s_sub_i32 s26, s79, s6
	s_cmp_ge_i32 s80, s26
	s_mov_b64 s[4:5], -1
	s_cbranch_scc0 .LBB0_207
	s_and_b64 s[2:3], s[2:3], exec
	s_cselect_b32 s8, 0x35c2, 0
	s_sub_i32 s2, s80, s26
	s_lshl_b32 s2, s2, 3
	v_readlane_b32 s3, v253, 7
	s_add_i32 s2, s2, s3
	s_cmp_ge_u32 s2, s8
	s_cbranch_scc1 .LBB0_206
	s_lshl_b32 s7, s6, 3
	s_load_dwordx2 s[20:21], s[88:89], 0x98
	s_load_dwordx2 s[22:23], s[88:89], 0xa8
	s_load_dwordx2 s[24:25], s[88:89], 0xb8
	s_add_u32 s28, s86, 0x3000000
	s_addc_u32 s29, s87, 0
	s_add_i32 s9, s8, -1
	s_mov_b32 s10, s2
	s_mov_b32 s11, s2
	s_mov_b32 s30, 0x42800000
	v_lshlrev_b32_e32 v1, 4, v162
	v_and_b32_e32 v2, 15, v162
	v_lshlrev_b32_e32 v2, 6, v2
	v_lshrrev_b32_e32 v3, 4, v162
	v_lshl_add_u32 v2, v3, 4, v2
	v_add_u32_e32 v148, 0x2000, v1
	v_add_u32_e32 v149, 0x4000, v1
	v_add_u32_e32 v150, 0x6000, v1
	v_add_u32_e32 v151, 0x8000, v1
	v_add_u32_e32 v152, 0xa000, v1
	v_add_u32_e32 v153, 0xc000, v1
	v_add_u32_e32 v154, 0xe000, v1
	v_add_u32_e32 v155, 0x10000, v1
	v_add_u32_e32 v156, 0x12000, v1
	v_add_u32_e32 v157, 0x14000, v1
	v_add_u32_e32 v158, 0x16000, v1
	v_add_u32_e32 v228, 0x18000, v1
	v_add_u32_e32 v229, 0x1a000, v1
	v_add_u32_e32 v230, 0x1c000, v1
	v_add_u32_e32 v231, 0x1e000, v1
	s_waitcnt lgkmcnt(0)
	s_min_u32 s12, s10, s9
	s_lshr_b32 s13, s12, 15
	s_sub_u32 s13, 2, s13
	s_and_b32 s14, s12, 0x7fff
	s_lshr_b32 s15, s14, 3
	s_lshl_b32 s15, s15, 17
	s_and_b32 s14, s12, 7
	s_lshl_b32 s14, s14, 10
	s_or_b32 s15, s15, s14
	s_cmp_eq_u32 s13, 0
	s_cselect_b32 s16, s20, s22
	s_cselect_b32 s17, s21, s23
	s_cmp_eq_u32 s13, 2
	s_cselect_b32 s16, s24, s16
	s_cselect_b32 s17, s25, s17
	s_add_u32 s16, s16, s15
	s_addc_u32 s17, s17, 0
	global_load_dwordx4 v[4:7], v1, s[16:17] nt
	global_load_dwordx4 v[8:11], v148, s[16:17] nt
	global_load_dwordx4 v[12:15], v149, s[16:17] nt
	global_load_dwordx4 v[16:19], v150, s[16:17] nt
	global_load_dwordx4 v[20:23], v151, s[16:17] nt
	global_load_dwordx4 v[24:27], v152, s[16:17] nt
	global_load_dwordx4 v[28:31], v153, s[16:17] nt
	global_load_dwordx4 v[32:35], v154, s[16:17] nt
	global_load_dwordx4 v[36:39], v155, s[16:17] nt
	global_load_dwordx4 v[40:43], v156, s[16:17] nt
	global_load_dwordx4 v[44:47], v157, s[16:17] nt
	global_load_dwordx4 v[48:51], v158, s[16:17] nt
	global_load_dwordx4 v[52:55], v228, s[16:17] nt
	global_load_dwordx4 v[56:59], v229, s[16:17] nt
	global_load_dwordx4 v[60:63], v230, s[16:17] nt
	global_load_dwordx4 v[64:67], v231, s[16:17] nt
	s_add_u32 s10, s10, s7
	s_min_u32 s12, s10, s9
	s_lshr_b32 s13, s12, 15
	s_sub_u32 s13, 2, s13
	s_and_b32 s14, s12, 0x7fff
	s_lshr_b32 s15, s14, 3
	s_lshl_b32 s15, s15, 17
	s_and_b32 s14, s12, 7
	s_lshl_b32 s14, s14, 10
	s_or_b32 s15, s15, s14
	s_cmp_eq_u32 s13, 0
	s_cselect_b32 s16, s20, s22
	s_cselect_b32 s17, s21, s23
	s_cmp_eq_u32 s13, 2
	s_cselect_b32 s16, s24, s16
	s_cselect_b32 s17, s25, s17
	s_add_u32 s16, s16, s15
	s_addc_u32 s17, s17, 0
	global_load_dwordx4 v[68:71], v1, s[16:17] nt
	global_load_dwordx4 v[72:75], v148, s[16:17] nt
	global_load_dwordx4 v[76:79], v149, s[16:17] nt
	global_load_dwordx4 v[80:83], v150, s[16:17] nt
	global_load_dwordx4 v[84:87], v151, s[16:17] nt
	global_load_dwordx4 v[88:91], v152, s[16:17] nt
	global_load_dwordx4 v[92:95], v153, s[16:17] nt
	global_load_dwordx4 v[96:99], v154, s[16:17] nt
	global_load_dwordx4 v[100:103], v155, s[16:17] nt
	global_load_dwordx4 v[104:107], v156, s[16:17] nt
	global_load_dwordx4 v[108:111], v157, s[16:17] nt
	global_load_dwordx4 v[112:115], v158, s[16:17] nt
	global_load_dwordx4 v[116:119], v228, s[16:17] nt
	global_load_dwordx4 v[120:123], v229, s[16:17] nt
	global_load_dwordx4 v[124:127], v230, s[16:17] nt
	global_load_dwordx4 v[128:131], v231, s[16:17] nt
	s_add_u32 s10, s10, s7
	s_min_u32 s12, s10, s9
	s_lshr_b32 s13, s12, 15
	s_sub_u32 s13, 2, s13
	s_and_b32 s14, s12, 0x7fff
	s_lshr_b32 s15, s14, 3
	s_lshl_b32 s15, s15, 17
	s_and_b32 s14, s12, 7
	s_lshl_b32 s14, s14, 10
	s_or_b32 s15, s15, s14
	s_cmp_eq_u32 s13, 0
	s_cselect_b32 s16, s20, s22
	s_cselect_b32 s17, s21, s23
	s_cmp_eq_u32 s13, 2
	s_cselect_b32 s16, s24, s16
	s_cselect_b32 s17, s25, s17
	s_add_u32 s16, s16, s15
	s_addc_u32 s17, s17, 0
	global_load_dwordx4 v[164:167], v1, s[16:17] nt
	global_load_dwordx4 v[168:171], v148, s[16:17] nt
	global_load_dwordx4 v[172:175], v149, s[16:17] nt
	global_load_dwordx4 v[176:179], v150, s[16:17] nt
	global_load_dwordx4 v[180:183], v151, s[16:17] nt
	global_load_dwordx4 v[184:187], v152, s[16:17] nt
	global_load_dwordx4 v[188:191], v153, s[16:17] nt
	global_load_dwordx4 v[192:195], v154, s[16:17] nt
	global_load_dwordx4 v[196:199], v155, s[16:17] nt
	global_load_dwordx4 v[200:203], v156, s[16:17] nt
	global_load_dwordx4 v[204:207], v157, s[16:17] nt
	global_load_dwordx4 v[208:211], v158, s[16:17] nt
	global_load_dwordx4 v[212:215], v228, s[16:17] nt
	global_load_dwordx4 v[216:219], v229, s[16:17] nt
	global_load_dwordx4 v[220:223], v230, s[16:17] nt
	global_load_dwordx4 v[224:227], v231, s[16:17] nt
	s_add_u32 s10, s10, s7
; __device__ __forceinline__ unsigned pk_fp8x4(float a, float b, float c, float d) { int w = __builtin_amdgcn_cvt_pk_fp8_f32(a, b, 0, false); w = __builtin_amdgcn_cvt_pk_fp8_f32(c, d, w, true); return (unsigned)w; }
; __device__ __forceinline__ void convert_load(Frame& F, int it, f32x4 (&v)[16]) {
;     const int mat = it / TI_PER_MAT, r = it % TI_PER_MAT, type = mat / NE, e = mat % NE, kb = r >> 3, n4 = (r & 7) * 256 + F.lane * 4;
;     const float* src = F.in[type == 0 ? I_WGATE : (type == 1 ? I_WUP : I_WDOWN)] + (size_t)e * D * D + (size_t)(kb * 16) * D + n4;
; #pragma unroll
;     for (int i = 0; i < 16; ++i) v[i] = __builtin_nontemporal_load((const f32x4*)(src + (size_t)i * D));
; }
; __device__ __forceinline__ void convert_store(Frame& F, int it, const f32x4 (&v)[16]) {
;     const int mat = it / TI_PER_MAT, r = it % TI_PER_MAT, type = mat / NE, e = mat % NE, kb = r >> 3, n4 = (r & 7) * 256 + F.lane * 4;
;     unsigned char* dst = F.ws + (type == 0 ? WS_WG : (type == 1 ? WS_WU : WS_WD)) + (size_t)e * D * D + ((size_t)kb * D + n4) * 16;
; #pragma unroll
;     for (int nn = 0; nn < 4; ++nn)
;         *(u32x4*)(dst + nn * 16) = (u32x4){pk_fp8x4(v[0][nn] * W8_SCALE, v[1][nn] * W8_SCALE, v[2][nn] * W8_SCALE, v[3][nn] * W8_SCALE), pk_fp8x4(v[4][nn] * W8_SCALE, v[5][nn] * W8_SCALE, v[6][nn] * W8_SCALE, v[7][nn] * W8_SCALE),
;                                           pk_fp8x4(v[8][nn] * W8_SCALE, v[9][nn] * W8_SCALE, v[10][nn] * W8_SCALE, v[11][nn] * W8_SCALE), pk_fp8x4(v[12][nn] * W8_SCALE, v[13][nn] * W8_SCALE, v[14][nn] * W8_SCALE, v[15][nn] * W8_SCALE)};
; }
; __device__ __forceinline__ void convert_experts(Frame& F, int gw, int NGW, int it0, int it1) {
;     f32x4 A[16], B[16];
;     for (int it = it0 + gw; it < it1; it += 2 * NGW) {
;         const int i2 = it + NGW; const bool h2 = i2 < it1;
;         convert_load(F, it, A); convert_load(F, h2 ? i2 : it, B); __builtin_amdgcn_sched_barrier(0);
;         convert_store(F, it, A);
;         if (h2) convert_store(F, i2, B);
.Lcv2_p0:
	s_cmp_ge_u32 s11, s8
	s_cbranch_scc1 .Lcv2_done
	s_lshr_b32 s13, s11, 15
	s_sub_u32 s13, 2, s13
	s_and_b32 s14, s11, 0x7fff
	s_lshr_b32 s14, s14, 3
	s_lshl_b32 s14, s14, 15
	s_and_b32 s15, s11, 7
	s_lshl_b32 s15, s15, 12
	s_or_b32 s14, s14, s15
	s_lshl_b32 s13, s13, 28
	s_add_u32 s14, s14, s13
	s_add_u32 s18, s28, s14
	s_addc_u32 s19, s29, 0
	s_waitcnt vmcnt(32)
	v_mul_f32_e32 v4, s30, v4
	v_mul_f32_e32 v8, s30, v8
	v_mul_f32_e32 v12, s30, v12
	v_mul_f32_e32 v16, s30, v16
	v_mul_f32_e32 v20, s30, v20
	v_mul_f32_e32 v24, s30, v24
	v_cvt_pk_fp8_f32 v132, v4, v8
	v_mul_f32_e32 v28, s30, v28
	v_mul_f32_e32 v32, s30, v32
	v_cvt_pk_fp8_f32 v132, v12, v16 op_sel:[0,0,1]
	v_mul_f32_e32 v36, s30, v36
	v_mul_f32_e32 v40, s30, v40
	v_cvt_pk_fp8_f32 v133, v20, v24
	v_mul_f32_e32 v44, s30, v44
	v_mul_f32_e32 v48, s30, v48
	v_cvt_pk_fp8_f32 v133, v28, v32 op_sel:[0,0,1]
	v_mul_f32_e32 v52, s30, v52
	v_mul_f32_e32 v56, s30, v56
	v_cvt_pk_fp8_f32 v134, v36, v40
	v_mul_f32_e32 v60, s30, v60
	v_mul_f32_e32 v64, s30, v64
	v_cvt_pk_fp8_f32 v134, v44, v48 op_sel:[0,0,1]
	v_mul_f32_e32 v5, s30, v5
	v_mul_f32_e32 v9, s30, v9
	v_cvt_pk_fp8_f32 v135, v52, v56
	v_mul_f32_e32 v13, s30, v13
	v_mul_f32_e32 v17, s30, v17
	v_cvt_pk_fp8_f32 v135, v60, v64 op_sel:[0,0,1]
	v_mul_f32_e32 v21, s30, v21
	v_mul_f32_e32 v25, s30, v25
	v_cvt_pk_fp8_f32 v136, v5, v9
	v_mul_f32_e32 v29, s30, v29
	v_mul_f32_e32 v33, s30, v33
	v_cvt_pk_fp8_f32 v136, v13, v17 op_sel:[0,0,1]
	v_mul_f32_e32 v37, s30, v37
	v_mul_f32_e32 v41, s30, v41
	v_cvt_pk_fp8_f32 v137, v21, v25
	v_mul_f32_e32 v45, s30, v45
	v_mul_f32_e32 v49, s30, v49
	v_cvt_pk_fp8_f32 v137, v29, v33 op_sel:[0,0,1]
	v_mul_f32_e32 v53, s30, v53
	v_mul_f32_e32 v57, s30, v57
	v_cvt_pk_fp8_f32 v138, v37, v41
	v_mul_f32_e32 v61, s30, v61
	v_mul_f32_e32 v65, s30, v65
	v_cvt_pk_fp8_f32 v138, v45, v49 op_sel:[0,0,1]
	v_mul_f32_e32 v6, s30, v6
	v_mul_f32_e32 v10, s30, v10
	v_cvt_pk_fp8_f32 v139, v53, v57
	v_mul_f32_e32 v14, s30, v14
	v_mul_f32_e32 v18, s30, v18
	v_cvt_pk_fp8_f32 v139, v61, v65 op_sel:[0,0,1]
	v_mul_f32_e32 v22, s30, v22
	v_mul_f32_e32 v26, s30, v26
	v_cvt_pk_fp8_f32 v140, v6, v10
	v_mul_f32_e32 v30, s30, v30
	v_mul_f32_e32 v34, s30, v34
	v_cvt_pk_fp8_f32 v140, v14, v18 op_sel:[0,0,1]
	v_mul_f32_e32 v38, s30, v38
	v_mul_f32_e32 v42, s30, v42
	v_cvt_pk_fp8_f32 v141, v22, v26
	v_mul_f32_e32 v46, s30, v46
	v_mul_f32_e32 v50, s30, v50
	v_cvt_pk_fp8_f32 v141, v30, v34 op_sel:[0,0,1]
	v_mul_f32_e32 v54, s30, v54
	v_mul_f32_e32 v58, s30, v58
	v_cvt_pk_fp8_f32 v142, v38, v42
	v_mul_f32_e32 v62, s30, v62
	v_mul_f32_e32 v66, s30, v66
	v_cvt_pk_fp8_f32 v142, v46, v50 op_sel:[0,0,1]
	v_mul_f32_e32 v7, s30, v7
	v_mul_f32_e32 v11, s30, v11
	v_cvt_pk_fp8_f32 v143, v54, v58
	v_mul_f32_e32 v15, s30, v15
	v_mul_f32_e32 v19, s30, v19
	v_cvt_pk_fp8_f32 v143, v62, v66 op_sel:[0,0,1]
	v_mul_f32_e32 v23, s30, v23
	v_mul_f32_e32 v27, s30, v27
	v_cvt_pk_fp8_f32 v144, v7, v11
	v_mul_f32_e32 v31, s30, v31
	v_mul_f32_e32 v35, s30, v35
	v_cvt_pk_fp8_f32 v144, v15, v19 op_sel:[0,0,1]
	v_mul_f32_e32 v39, s30, v39
	v_mul_f32_e32 v43, s30, v43
	v_cvt_pk_fp8_f32 v145, v23, v27
	v_mul_f32_e32 v47, s30, v47
	v_mul_f32_e32 v51, s30, v51
	v_cvt_pk_fp8_f32 v145, v31, v35 op_sel:[0,0,1]
	v_mul_f32_e32 v55, s30, v55
	v_mul_f32_e32 v59, s30, v59
	v_cvt_pk_fp8_f32 v146, v39, v43
	v_mul_f32_e32 v63, s30, v63
	v_mul_f32_e32 v67, s30, v67
	v_cvt_pk_fp8_f32 v146, v47, v51 op_sel:[0,0,1]
	v_cvt_pk_fp8_f32 v147, v55, v59
	s_add_u32 s11, s11, s7
	v_cvt_pk_fp8_f32 v147, v63, v67 op_sel:[0,0,1]
	s_nop 1
	v_permlane32_swap_b32_e32 v132, v140
	v_permlane32_swap_b32_e32 v133, v141
	v_permlane32_swap_b32_e32 v134, v142
	v_permlane32_swap_b32_e32 v135, v143
	v_permlane32_swap_b32_e32 v136, v144
	v_permlane32_swap_b32_e32 v137, v145
	v_permlane32_swap_b32_e32 v138, v146
	v_permlane32_swap_b32_e32 v139, v147
	v_permlane16_swap_b32_e32 v132, v136
	v_permlane16_swap_b32_e32 v133, v137
	v_permlane16_swap_b32_e32 v134, v138
	v_permlane16_swap_b32_e32 v135, v139
	v_permlane16_swap_b32_e32 v140, v144
	v_permlane16_swap_b32_e32 v141, v145
	v_permlane16_swap_b32_e32 v142, v146
	v_permlane16_swap_b32_e32 v143, v147
	global_store_dwordx4 v2, v[132:135], s[18:19]
	global_store_dwordx4 v2, v[136:139], s[18:19] offset:1024
	global_store_dwordx4 v2, v[140:143], s[18:19] offset:2048
	global_store_dwordx4 v2, v[144:147], s[18:19] offset:3072
	s_min_u32 s12, s10, s9
	s_lshr_b32 s13, s12, 15
	s_sub_u32 s13, 2, s13
	s_and_b32 s14, s12, 0x7fff
	s_lshr_b32 s15, s14, 3
	s_lshl_b32 s15, s15, 17
	s_and_b32 s14, s12, 7
	s_lshl_b32 s14, s14, 10
	s_or_b32 s15, s15, s14
	s_cmp_eq_u32 s13, 0
	s_cselect_b32 s16, s20, s22
	s_cselect_b32 s17, s21, s23
	s_cmp_eq_u32 s13, 2
	s_cselect_b32 s16, s24, s16
	s_cselect_b32 s17, s25, s17
	s_add_u32 s16, s16, s15
	s_addc_u32 s17, s17, 0
	global_load_dwordx4 v[4:7], v1, s[16:17] nt
	global_load_dwordx4 v[8:11], v148, s[16:17] nt
	global_load_dwordx4 v[12:15], v149, s[16:17] nt
	global_load_dwordx4 v[16:19], v150, s[16:17] nt
	global_load_dwordx4 v[20:23], v151, s[16:17] nt
	global_load_dwordx4 v[24:27], v152, s[16:17] nt
	global_load_dwordx4 v[28:31], v153, s[16:17] nt
	global_load_dwordx4 v[32:35], v154, s[16:17] nt
	global_load_dwordx4 v[36:39], v155, s[16:17] nt
	global_load_dwordx4 v[40:43], v156, s[16:17] nt
	global_load_dwordx4 v[44:47], v157, s[16:17] nt
	global_load_dwordx4 v[48:51], v158, s[16:17] nt
	global_load_dwordx4 v[52:55], v228, s[16:17] nt
	global_load_dwordx4 v[56:59], v229, s[16:17] nt
	global_load_dwordx4 v[60:63], v230, s[16:17] nt
	global_load_dwordx4 v[64:67], v231, s[16:17] nt
	s_add_u32 s10, s10, s7
; __device__ __forceinline__ unsigned pk_fp8x4(float a, float b, float c, float d) { int w = __builtin_amdgcn_cvt_pk_fp8_f32(a, b, 0, false); w = __builtin_amdgcn_cvt_pk_fp8_f32(c, d, w, true); return (unsigned)w; }
; __device__ __forceinline__ void convert_load(Frame& F, int it, f32x4 (&v)[16]) {
;     const int mat = it / TI_PER_MAT, r = it % TI_PER_MAT, type = mat / NE, e = mat % NE, kb = r >> 3, n4 = (r & 7) * 256 + F.lane * 4;
;     const float* src = F.in[type == 0 ? I_WGATE : (type == 1 ? I_WUP : I_WDOWN)] + (size_t)e * D * D + (size_t)(kb * 16) * D + n4;
; #pragma unroll
;     for (int i = 0; i < 16; ++i) v[i] = __builtin_nontemporal_load((const f32x4*)(src + (size_t)i * D));
; }
; __device__ __forceinline__ void convert_store(Frame& F, int it, const f32x4 (&v)[16]) {
;     const int mat = it / TI_PER_MAT, r = it % TI_PER_MAT, type = mat / NE, e = mat % NE, kb = r >> 3, n4 = (r & 7) * 256 + F.lane * 4;
;     unsigned char* dst = F.ws + (type == 0 ? WS_WG : (type == 1 ? WS_WU : WS_WD)) + (size_t)e * D * D + ((size_t)kb * D + n4) * 16;
; #pragma unroll
;     for (int nn = 0; nn < 4; ++nn)
;         *(u32x4*)(dst + nn * 16) = (u32x4){pk_fp8x4(v[0][nn] * W8_SCALE, v[1][nn] * W8_SCALE, v[2][nn] * W8_SCALE, v[3][nn] * W8_SCALE), pk_fp8x4(v[4][nn] * W8_SCALE, v[5][nn] * W8_SCALE, v[6][nn] * W8_SCALE, v[7][nn] * W8_SCALE),
;                                           pk_fp8x4(v[8][nn] * W8_SCALE, v[9][nn] * W8_SCALE, v[10][nn] * W8_SCALE, v[11][nn] * W8_SCALE), pk_fp8x4(v[12][nn] * W8_SCALE, v[13][nn] * W8_SCALE, v[14][nn] * W8_SCALE, v[15][nn] * W8_SCALE)};
; }
; __device__ __forceinline__ void convert_experts(Frame& F, int gw, int NGW, int it0, int it1) {
;     f32x4 A[16], B[16];
;     for (int it = it0 + gw; it < it1; it += 2 * NGW) {
;         const int i2 = it + NGW; const bool h2 = i2 < it1;
;         convert_load(F, it, A); convert_load(F, h2 ? i2 : it, B); __builtin_amdgcn_sched_barrier(0);
;         convert_store(F, it, A);
;         if (h2) convert_store(F, i2, B);
.Lcv2_p1:
	s_cmp_ge_u32 s11, s8
	s_cbranch_scc1 .Lcv2_done
	s_lshr_b32 s13, s11, 15
	s_sub_u32 s13, 2, s13
	s_and_b32 s14, s11, 0x7fff
	s_lshr_b32 s14, s14, 3
	s_lshl_b32 s14, s14, 15
	s_and_b32 s15, s11, 7
	s_lshl_b32 s15, s15, 12
	s_or_b32 s14, s14, s15
	s_lshl_b32 s13, s13, 28
	s_add_u32 s14, s14, s13
	s_add_u32 s18, s28, s14
	s_addc_u32 s19, s29, 0
	s_waitcnt vmcnt(36)
	v_mul_f32_e32 v68, s30, v68
	v_mul_f32_e32 v72, s30, v72
	v_mul_f32_e32 v76, s30, v76
	v_mul_f32_e32 v80, s30, v80
	v_mul_f32_e32 v84, s30, v84
	v_mul_f32_e32 v88, s30, v88
	v_cvt_pk_fp8_f32 v132, v68, v72
	v_mul_f32_e32 v92, s30, v92
	v_mul_f32_e32 v96, s30, v96
	v_cvt_pk_fp8_f32 v132, v76, v80 op_sel:[0,0,1]
	v_mul_f32_e32 v100, s30, v100
	v_mul_f32_e32 v104, s30, v104
	v_cvt_pk_fp8_f32 v133, v84, v88
	v_mul_f32_e32 v108, s30, v108
	v_mul_f32_e32 v112, s30, v112
	v_cvt_pk_fp8_f32 v133, v92, v96 op_sel:[0,0,1]
	v_mul_f32_e32 v116, s30, v116
	v_mul_f32_e32 v120, s30, v120
	v_cvt_pk_fp8_f32 v134, v100, v104
	v_mul_f32_e32 v124, s30, v124
	v_mul_f32_e32 v128, s30, v128
	v_cvt_pk_fp8_f32 v134, v108, v112 op_sel:[0,0,1]
	v_mul_f32_e32 v69, s30, v69
	v_mul_f32_e32 v73, s30, v73
	v_cvt_pk_fp8_f32 v135, v116, v120
	v_mul_f32_e32 v77, s30, v77
	v_mul_f32_e32 v81, s30, v81
	v_cvt_pk_fp8_f32 v135, v124, v128 op_sel:[0,0,1]
	v_mul_f32_e32 v85, s30, v85
	v_mul_f32_e32 v89, s30, v89
	v_cvt_pk_fp8_f32 v136, v69, v73
	v_mul_f32_e32 v93, s30, v93
	v_mul_f32_e32 v97, s30, v97
	v_cvt_pk_fp8_f32 v136, v77, v81 op_sel:[0,0,1]
	v_mul_f32_e32 v101, s30, v101
	v_mul_f32_e32 v105, s30, v105
	v_cvt_pk_fp8_f32 v137, v85, v89
	v_mul_f32_e32 v109, s30, v109
	v_mul_f32_e32 v113, s30, v113
	v_cvt_pk_fp8_f32 v137, v93, v97 op_sel:[0,0,1]
	v_mul_f32_e32 v117, s30, v117
	v_mul_f32_e32 v121, s30, v121
	v_cvt_pk_fp8_f32 v138, v101, v105
	v_mul_f32_e32 v125, s30, v125
	v_mul_f32_e32 v129, s30, v129
	v_cvt_pk_fp8_f32 v138, v109, v113 op_sel:[0,0,1]
	v_mul_f32_e32 v70, s30, v70
	v_mul_f32_e32 v74, s30, v74
	v_cvt_pk_fp8_f32 v139, v117, v121
	v_mul_f32_e32 v78, s30, v78
	v_mul_f32_e32 v82, s30, v82
	v_cvt_pk_fp8_f32 v139, v125, v129 op_sel:[0,0,1]
	v_mul_f32_e32 v86, s30, v86
	v_mul_f32_e32 v90, s30, v90
	v_cvt_pk_fp8_f32 v140, v70, v74
	v_mul_f32_e32 v94, s30, v94
	v_mul_f32_e32 v98, s30, v98
	v_cvt_pk_fp8_f32 v140, v78, v82 op_sel:[0,0,1]
	v_mul_f32_e32 v102, s30, v102
	v_mul_f32_e32 v106, s30, v106
	v_cvt_pk_fp8_f32 v141, v86, v90
	v_mul_f32_e32 v110, s30, v110
	v_mul_f32_e32 v114, s30, v114
	v_cvt_pk_fp8_f32 v141, v94, v98 op_sel:[0,0,1]
	v_mul_f32_e32 v118, s30, v118
	v_mul_f32_e32 v122, s30, v122
	v_cvt_pk_fp8_f32 v142, v102, v106
	v_mul_f32_e32 v126, s30, v126
	v_mul_f32_e32 v130, s30, v130
	v_cvt_pk_fp8_f32 v142, v110, v114 op_sel:[0,0,1]
	v_mul_f32_e32 v71, s30, v71
	v_mul_f32_e32 v75, s30, v75
	v_cvt_pk_fp8_f32 v143, v118, v122
	v_mul_f32_e32 v79, s30, v79
	v_mul_f32_e32 v83, s30, v83
	v_cvt_pk_fp8_f32 v143, v126, v130 op_sel:[0,0,1]
	v_mul_f32_e32 v87, s30, v87
	v_mul_f32_e32 v91, s30, v91
	v_cvt_pk_fp8_f32 v144, v71, v75
	v_mul_f32_e32 v95, s30, v95
	v_mul_f32_e32 v99, s30, v99
	v_cvt_pk_fp8_f32 v144, v79, v83 op_sel:[0,0,1]
	v_mul_f32_e32 v103, s30, v103
	v_mul_f32_e32 v107, s30, v107
	v_cvt_pk_fp8_f32 v145, v87, v91
	v_mul_f32_e32 v111, s30, v111
	v_mul_f32_e32 v115, s30, v115
	v_cvt_pk_fp8_f32 v145, v95, v99 op_sel:[0,0,1]
	v_mul_f32_e32 v119, s30, v119
	v_mul_f32_e32 v123, s30, v123
	v_cvt_pk_fp8_f32 v146, v103, v107
	v_mul_f32_e32 v127, s30, v127
	v_mul_f32_e32 v131, s30, v131
	v_cvt_pk_fp8_f32 v146, v111, v115 op_sel:[0,0,1]
	v_cvt_pk_fp8_f32 v147, v119, v123
	s_add_u32 s11, s11, s7
	v_cvt_pk_fp8_f32 v147, v127, v131 op_sel:[0,0,1]
	s_nop 1
	v_permlane32_swap_b32_e32 v132, v140
	v_permlane32_swap_b32_e32 v133, v141
	v_permlane32_swap_b32_e32 v134, v142
	v_permlane32_swap_b32_e32 v135, v143
	v_permlane32_swap_b32_e32 v136, v144
	v_permlane32_swap_b32_e32 v137, v145
	v_permlane32_swap_b32_e32 v138, v146
	v_permlane32_swap_b32_e32 v139, v147
	v_permlane16_swap_b32_e32 v132, v136
	v_permlane16_swap_b32_e32 v133, v137
	v_permlane16_swap_b32_e32 v134, v138
	v_permlane16_swap_b32_e32 v135, v139
	v_permlane16_swap_b32_e32 v140, v144
	v_permlane16_swap_b32_e32 v141, v145
	v_permlane16_swap_b32_e32 v142, v146
	v_permlane16_swap_b32_e32 v143, v147
	global_store_dwordx4 v2, v[132:135], s[18:19]
	global_store_dwordx4 v2, v[136:139], s[18:19] offset:1024
	global_store_dwordx4 v2, v[140:143], s[18:19] offset:2048
	global_store_dwordx4 v2, v[144:147], s[18:19] offset:3072
	s_min_u32 s12, s10, s9
	s_lshr_b32 s13, s12, 15
	s_sub_u32 s13, 2, s13
	s_and_b32 s14, s12, 0x7fff
	s_lshr_b32 s15, s14, 3
	s_lshl_b32 s15, s15, 17
	s_and_b32 s14, s12, 7
	s_lshl_b32 s14, s14, 10
	s_or_b32 s15, s15, s14
	s_cmp_eq_u32 s13, 0
	s_cselect_b32 s16, s20, s22
	s_cselect_b32 s17, s21, s23
	s_cmp_eq_u32 s13, 2
	s_cselect_b32 s16, s24, s16
	s_cselect_b32 s17, s25, s17
	s_add_u32 s16, s16, s15
	s_addc_u32 s17, s17, 0
	global_load_dwordx4 v[68:71], v1, s[16:17] nt
	global_load_dwordx4 v[72:75], v148, s[16:17] nt
	global_load_dwordx4 v[76:79], v149, s[16:17] nt
	global_load_dwordx4 v[80:83], v150, s[16:17] nt
	global_load_dwordx4 v[84:87], v151, s[16:17] nt
	global_load_dwordx4 v[88:91], v152, s[16:17] nt
	global_load_dwordx4 v[92:95], v153, s[16:17] nt
	global_load_dwordx4 v[96:99], v154, s[16:17] nt
	global_load_dwordx4 v[100:103], v155, s[16:17] nt
	global_load_dwordx4 v[104:107], v156, s[16:17] nt
	global_load_dwordx4 v[108:111], v157, s[16:17] nt
	global_load_dwordx4 v[112:115], v158, s[16:17] nt
	global_load_dwordx4 v[116:119], v228, s[16:17] nt
	global_load_dwordx4 v[120:123], v229, s[16:17] nt
	global_load_dwordx4 v[124:127], v230, s[16:17] nt
	global_load_dwordx4 v[128:131], v231, s[16:17] nt
	s_add_u32 s10, s10, s7
; __device__ __forceinline__ unsigned pk_fp8x4(float a, float b, float c, float d) { int w = __builtin_amdgcn_cvt_pk_fp8_f32(a, b, 0, false); w = __builtin_amdgcn_cvt_pk_fp8_f32(c, d, w, true); return (unsigned)w; }
; __device__ __forceinline__ void convert_load(Frame& F, int it, f32x4 (&v)[16]) {
;     const int mat = it / TI_PER_MAT, r = it % TI_PER_MAT, type = mat / NE, e = mat % NE, kb = r >> 3, n4 = (r & 7) * 256 + F.lane * 4;
;     const float* src = F.in[type == 0 ? I_WGATE : (type == 1 ? I_WUP : I_WDOWN)] + (size_t)e * D * D + (size_t)(kb * 16) * D + n4;
; #pragma unroll
;     for (int i = 0; i < 16; ++i) v[i] = __builtin_nontemporal_load((const f32x4*)(src + (size_t)i * D));
; }
; __device__ __forceinline__ void convert_store(Frame& F, int it, const f32x4 (&v)[16]) {
;     const int mat = it / TI_PER_MAT, r = it % TI_PER_MAT, type = mat / NE, e = mat % NE, kb = r >> 3, n4 = (r & 7) * 256 + F.lane * 4;
;     unsigned char* dst = F.ws + (type == 0 ? WS_WG : (type == 1 ? WS_WU : WS_WD)) + (size_t)e * D * D + ((size_t)kb * D + n4) * 16;
; #pragma unroll
;     for (int nn = 0; nn < 4; ++nn)
;         *(u32x4*)(dst + nn * 16) = (u32x4){pk_fp8x4(v[0][nn] * W8_SCALE, v[1][nn] * W8_SCALE, v[2][nn] * W8_SCALE, v[3][nn] * W8_SCALE), pk_fp8x4(v[4][nn] * W8_SCALE, v[5][nn] * W8_SCALE, v[6][nn] * W8_SCALE, v[7][nn] * W8_SCALE),
;                                           pk_fp8x4(v[8][nn] * W8_SCALE, v[9][nn] * W8_SCALE, v[10][nn] * W8_SCALE, v[11][nn] * W8_SCALE), pk_fp8x4(v[12][nn] * W8_SCALE, v[13][nn] * W8_SCALE, v[14][nn] * W8_SCALE, v[15][nn] * W8_SCALE)};
; }
; __device__ __forceinline__ void convert_experts(Frame& F, int gw, int NGW, int it0, int it1) {
;     f32x4 A[16], B[16];
;     for (int it = it0 + gw; it < it1; it += 2 * NGW) {
;         const int i2 = it + NGW; const bool h2 = i2 < it1;
;         convert_load(F, it, A); convert_load(F, h2 ? i2 : it, B); __builtin_amdgcn_sched_barrier(0);
;         convert_store(F, it, A);
;         if (h2) convert_store(F, i2, B);
.Lcv2_loop:
.Lcv2_l2:
	s_cmp_ge_u32 s11, s8
	s_cbranch_scc1 .Lcv2_done
	s_lshr_b32 s13, s11, 15
	s_sub_u32 s13, 2, s13
	s_and_b32 s14, s11, 0x7fff
	s_lshr_b32 s14, s14, 3
	s_lshl_b32 s14, s14, 15
	s_and_b32 s15, s11, 7
	s_lshl_b32 s15, s15, 12
	s_or_b32 s14, s14, s15
	s_lshl_b32 s13, s13, 28
	s_add_u32 s14, s14, s13
	s_add_u32 s18, s28, s14
	s_addc_u32 s19, s29, 0
	s_waitcnt vmcnt(40)
	v_mul_f32_e32 v164, s30, v164
	v_mul_f32_e32 v168, s30, v168
	v_mul_f32_e32 v172, s30, v172
	v_mul_f32_e32 v176, s30, v176
	v_mul_f32_e32 v180, s30, v180
	v_mul_f32_e32 v184, s30, v184
	v_cvt_pk_fp8_f32 v132, v164, v168
	v_mul_f32_e32 v188, s30, v188
	v_mul_f32_e32 v192, s30, v192
	v_cvt_pk_fp8_f32 v132, v172, v176 op_sel:[0,0,1]
	v_mul_f32_e32 v196, s30, v196
	v_mul_f32_e32 v200, s30, v200
	v_cvt_pk_fp8_f32 v133, v180, v184
	v_mul_f32_e32 v204, s30, v204
	v_mul_f32_e32 v208, s30, v208
	v_cvt_pk_fp8_f32 v133, v188, v192 op_sel:[0,0,1]
	v_mul_f32_e32 v212, s30, v212
	v_mul_f32_e32 v216, s30, v216
	v_cvt_pk_fp8_f32 v134, v196, v200
	v_mul_f32_e32 v220, s30, v220
	v_mul_f32_e32 v224, s30, v224
	v_cvt_pk_fp8_f32 v134, v204, v208 op_sel:[0,0,1]
	v_mul_f32_e32 v165, s30, v165
	v_mul_f32_e32 v169, s30, v169
	v_cvt_pk_fp8_f32 v135, v212, v216
	v_mul_f32_e32 v173, s30, v173
	v_mul_f32_e32 v177, s30, v177
	v_cvt_pk_fp8_f32 v135, v220, v224 op_sel:[0,0,1]
	v_mul_f32_e32 v181, s30, v181
	v_mul_f32_e32 v185, s30, v185
	v_cvt_pk_fp8_f32 v136, v165, v169
	v_mul_f32_e32 v189, s30, v189
	v_mul_f32_e32 v193, s30, v193
	v_cvt_pk_fp8_f32 v136, v173, v177 op_sel:[0,0,1]
	v_mul_f32_e32 v197, s30, v197
	v_mul_f32_e32 v201, s30, v201
	v_cvt_pk_fp8_f32 v137, v181, v185
	v_mul_f32_e32 v205, s30, v205
	v_mul_f32_e32 v209, s30, v209
	v_cvt_pk_fp8_f32 v137, v189, v193 op_sel:[0,0,1]
	v_mul_f32_e32 v213, s30, v213
	v_mul_f32_e32 v217, s30, v217
	v_cvt_pk_fp8_f32 v138, v197, v201
	v_mul_f32_e32 v221, s30, v221
	v_mul_f32_e32 v225, s30, v225
	v_cvt_pk_fp8_f32 v138, v205, v209 op_sel:[0,0,1]
	v_mul_f32_e32 v166, s30, v166
	v_mul_f32_e32 v170, s30, v170
	v_cvt_pk_fp8_f32 v139, v213, v217
	v_mul_f32_e32 v174, s30, v174
	v_mul_f32_e32 v178, s30, v178
	v_cvt_pk_fp8_f32 v139, v221, v225 op_sel:[0,0,1]
	v_mul_f32_e32 v182, s30, v182
	v_mul_f32_e32 v186, s30, v186
	v_cvt_pk_fp8_f32 v140, v166, v170
	v_mul_f32_e32 v190, s30, v190
	v_mul_f32_e32 v194, s30, v194
	v_cvt_pk_fp8_f32 v140, v174, v178 op_sel:[0,0,1]
	v_mul_f32_e32 v198, s30, v198
	v_mul_f32_e32 v202, s30, v202
	v_cvt_pk_fp8_f32 v141, v182, v186
	v_mul_f32_e32 v206, s30, v206
	v_mul_f32_e32 v210, s30, v210
	v_cvt_pk_fp8_f32 v141, v190, v194 op_sel:[0,0,1]
	v_mul_f32_e32 v214, s30, v214
	v_mul_f32_e32 v218, s30, v218
	v_cvt_pk_fp8_f32 v142, v198, v202
	v_mul_f32_e32 v222, s30, v222
	v_mul_f32_e32 v226, s30, v226
	v_cvt_pk_fp8_f32 v142, v206, v210 op_sel:[0,0,1]
	v_mul_f32_e32 v167, s30, v167
	v_mul_f32_e32 v171, s30, v171
	v_cvt_pk_fp8_f32 v143, v214, v218
	v_mul_f32_e32 v175, s30, v175
	v_mul_f32_e32 v179, s30, v179
	v_cvt_pk_fp8_f32 v143, v222, v226 op_sel:[0,0,1]
	v_mul_f32_e32 v183, s30, v183
	v_mul_f32_e32 v187, s30, v187
	v_cvt_pk_fp8_f32 v144, v167, v171
	v_mul_f32_e32 v191, s30, v191
	v_mul_f32_e32 v195, s30, v195
	v_cvt_pk_fp8_f32 v144, v175, v179 op_sel:[0,0,1]
	v_mul_f32_e32 v199, s30, v199
	v_mul_f32_e32 v203, s30, v203
	v_cvt_pk_fp8_f32 v145, v183, v187
	v_mul_f32_e32 v207, s30, v207
	v_mul_f32_e32 v211, s30, v211
	v_cvt_pk_fp8_f32 v145, v191, v195 op_sel:[0,0,1]
	v_mul_f32_e32 v215, s30, v215
	v_mul_f32_e32 v219, s30, v219
	v_cvt_pk_fp8_f32 v146, v199, v203
	v_mul_f32_e32 v223, s30, v223
	v_mul_f32_e32 v227, s30, v227
	v_cvt_pk_fp8_f32 v146, v207, v211 op_sel:[0,0,1]
	v_cvt_pk_fp8_f32 v147, v215, v219
	s_add_u32 s11, s11, s7
	v_cvt_pk_fp8_f32 v147, v223, v227 op_sel:[0,0,1]
	s_nop 1
	v_permlane32_swap_b32_e32 v132, v140
	v_permlane32_swap_b32_e32 v133, v141
	v_permlane32_swap_b32_e32 v134, v142
	v_permlane32_swap_b32_e32 v135, v143
	v_permlane32_swap_b32_e32 v136, v144
	v_permlane32_swap_b32_e32 v137, v145
	v_permlane32_swap_b32_e32 v138, v146
	v_permlane32_swap_b32_e32 v139, v147
	v_permlane16_swap_b32_e32 v132, v136
	v_permlane16_swap_b32_e32 v133, v137
	v_permlane16_swap_b32_e32 v134, v138
	v_permlane16_swap_b32_e32 v135, v139
	v_permlane16_swap_b32_e32 v140, v144
	v_permlane16_swap_b32_e32 v141, v145
	v_permlane16_swap_b32_e32 v142, v146
	v_permlane16_swap_b32_e32 v143, v147
	global_store_dwordx4 v2, v[132:135], s[18:19]
	global_store_dwordx4 v2, v[136:139], s[18:19] offset:1024
	global_store_dwordx4 v2, v[140:143], s[18:19] offset:2048
	global_store_dwordx4 v2, v[144:147], s[18:19] offset:3072
	s_min_u32 s12, s10, s9
	s_lshr_b32 s13, s12, 15
	s_sub_u32 s13, 2, s13
	s_and_b32 s14, s12, 0x7fff
	s_lshr_b32 s15, s14, 3
	s_lshl_b32 s15, s15, 17
	s_and_b32 s14, s12, 7
	s_lshl_b32 s14, s14, 10
	s_or_b32 s15, s15, s14
	s_cmp_eq_u32 s13, 0
	s_cselect_b32 s16, s20, s22
	s_cselect_b32 s17, s21, s23
	s_cmp_eq_u32 s13, 2
	s_cselect_b32 s16, s24, s16
	s_cselect_b32 s17, s25, s17
	s_add_u32 s16, s16, s15
	s_addc_u32 s17, s17, 0
	global_load_dwordx4 v[164:167], v1, s[16:17] nt
	global_load_dwordx4 v[168:171], v148, s[16:17] nt
	global_load_dwordx4 v[172:175], v149, s[16:17] nt
	global_load_dwordx4 v[176:179], v150, s[16:17] nt
	global_load_dwordx4 v[180:183], v151, s[16:17] nt
	global_load_dwordx4 v[184:187], v152, s[16:17] nt
	global_load_dwordx4 v[188:191], v153, s[16:17] nt
	global_load_dwordx4 v[192:195], v154, s[16:17] nt
	global_load_dwordx4 v[196:199], v155, s[16:17] nt
	global_load_dwordx4 v[200:203], v156, s[16:17] nt
	global_load_dwordx4 v[204:207], v157, s[16:17] nt
	global_load_dwordx4 v[208:211], v158, s[16:17] nt
	global_load_dwordx4 v[212:215], v228, s[16:17] nt
	global_load_dwordx4 v[216:219], v229, s[16:17] nt
	global_load_dwordx4 v[220:223], v230, s[16:17] nt
	global_load_dwordx4 v[224:227], v231, s[16:17] nt
	s_add_u32 s10, s10, s7
; __device__ __forceinline__ unsigned pk_fp8x4(float a, float b, float c, float d) { int w = __builtin_amdgcn_cvt_pk_fp8_f32(a, b, 0, false); w = __builtin_amdgcn_cvt_pk_fp8_f32(c, d, w, true); return (unsigned)w; }
; __device__ __forceinline__ void convert_load(Frame& F, int it, f32x4 (&v)[16]) {
;     const int mat = it / TI_PER_MAT, r = it % TI_PER_MAT, type = mat / NE, e = mat % NE, kb = r >> 3, n4 = (r & 7) * 256 + F.lane * 4;
;     const float* src = F.in[type == 0 ? I_WGATE : (type == 1 ? I_WUP : I_WDOWN)] + (size_t)e * D * D + (size_t)(kb * 16) * D + n4;
; #pragma unroll
;     for (int i = 0; i < 16; ++i) v[i] = __builtin_nontemporal_load((const f32x4*)(src + (size_t)i * D));
; }
; __device__ __forceinline__ void convert_store(Frame& F, int it, const f32x4 (&v)[16]) {
;     const int mat = it / TI_PER_MAT, r = it % TI_PER_MAT, type = mat / NE, e = mat % NE, kb = r >> 3, n4 = (r & 7) * 256 + F.lane * 4;
;     unsigned char* dst = F.ws + (type == 0 ? WS_WG : (type == 1 ? WS_WU : WS_WD)) + (size_t)e * D * D + ((size_t)kb * D + n4) * 16;
; #pragma unroll
;     for (int nn = 0; nn < 4; ++nn)
;         *(u32x4*)(dst + nn * 16) = (u32x4){pk_fp8x4(v[0][nn] * W8_SCALE, v[1][nn] * W8_SCALE, v[2][nn] * W8_SCALE, v[3][nn] * W8_SCALE), pk_fp8x4(v[4][nn] * W8_SCALE, v[5][nn] * W8_SCALE, v[6][nn] * W8_SCALE, v[7][nn] * W8_SCALE),
;                                           pk_fp8x4(v[8][nn] * W8_SCALE, v[9][nn] * W8_SCALE, v[10][nn] * W8_SCALE, v[11][nn] * W8_SCALE), pk_fp8x4(v[12][nn] * W8_SCALE, v[13][nn] * W8_SCALE, v[14][nn] * W8_SCALE, v[15][nn] * W8_SCALE)};
; }
; __device__ __forceinline__ void convert_experts(Frame& F, int gw, int NGW, int it0, int it1) {
;     f32x4 A[16], B[16];
;     for (int it = it0 + gw; it < it1; it += 2 * NGW) {
;         const int i2 = it + NGW; const bool h2 = i2 < it1;
;         convert_load(F, it, A); convert_load(F, h2 ? i2 : it, B); __builtin_amdgcn_sched_barrier(0);
;         convert_store(F, it, A);
;         if (h2) convert_store(F, i2, B);
.Lcv2_l0:
	s_cmp_ge_u32 s11, s8
	s_cbranch_scc1 .Lcv2_done
	s_lshr_b32 s13, s11, 15
	s_sub_u32 s13, 2, s13
	s_and_b32 s14, s11, 0x7fff
	s_lshr_b32 s14, s14, 3
	s_lshl_b32 s14, s14, 15
	s_and_b32 s15, s11, 7
	s_lshl_b32 s15, s15, 12
	s_or_b32 s14, s14, s15
	s_lshl_b32 s13, s13, 28
	s_add_u32 s14, s14, s13
	s_add_u32 s18, s28, s14
	s_addc_u32 s19, s29, 0
	s_waitcnt vmcnt(40)
	v_mul_f32_e32 v4, s30, v4
	v_mul_f32_e32 v8, s30, v8
	v_mul_f32_e32 v12, s30, v12
	v_mul_f32_e32 v16, s30, v16
	v_mul_f32_e32 v20, s30, v20
	v_mul_f32_e32 v24, s30, v24
	v_cvt_pk_fp8_f32 v132, v4, v8
	v_mul_f32_e32 v28, s30, v28
	v_mul_f32_e32 v32, s30, v32
	v_cvt_pk_fp8_f32 v132, v12, v16 op_sel:[0,0,1]
	v_mul_f32_e32 v36, s30, v36
	v_mul_f32_e32 v40, s30, v40
	v_cvt_pk_fp8_f32 v133, v20, v24
	v_mul_f32_e32 v44, s30, v44
	v_mul_f32_e32 v48, s30, v48
	v_cvt_pk_fp8_f32 v133, v28, v32 op_sel:[0,0,1]
	v_mul_f32_e32 v52, s30, v52
	v_mul_f32_e32 v56, s30, v56
	v_cvt_pk_fp8_f32 v134, v36, v40
	v_mul_f32_e32 v60, s30, v60
	v_mul_f32_e32 v64, s30, v64
	v_cvt_pk_fp8_f32 v134, v44, v48 op_sel:[0,0,1]
	v_mul_f32_e32 v5, s30, v5
	v_mul_f32_e32 v9, s30, v9
	v_cvt_pk_fp8_f32 v135, v52, v56
	v_mul_f32_e32 v13, s30, v13
	v_mul_f32_e32 v17, s30, v17
	v_cvt_pk_fp8_f32 v135, v60, v64 op_sel:[0,0,1]
	v_mul_f32_e32 v21, s30, v21
	v_mul_f32_e32 v25, s30, v25
	v_cvt_pk_fp8_f32 v136, v5, v9
	v_mul_f32_e32 v29, s30, v29
	v_mul_f32_e32 v33, s30, v33
	v_cvt_pk_fp8_f32 v136, v13, v17 op_sel:[0,0,1]
	v_mul_f32_e32 v37, s30, v37
	v_mul_f32_e32 v41, s30, v41
	v_cvt_pk_fp8_f32 v137, v21, v25
	v_mul_f32_e32 v45, s30, v45
	v_mul_f32_e32 v49, s30, v49
	v_cvt_pk_fp8_f32 v137, v29, v33 op_sel:[0,0,1]
	v_mul_f32_e32 v53, s30, v53
	v_mul_f32_e32 v57, s30, v57
	v_cvt_pk_fp8_f32 v138, v37, v41
	v_mul_f32_e32 v61, s30, v61
	v_mul_f32_e32 v65, s30, v65
	v_cvt_pk_fp8_f32 v138, v45, v49 op_sel:[0,0,1]
	v_mul_f32_e32 v6, s30, v6
	v_mul_f32_e32 v10, s30, v10
	v_cvt_pk_fp8_f32 v139, v53, v57
	v_mul_f32_e32 v14, s30, v14
	v_mul_f32_e32 v18, s30, v18
	v_cvt_pk_fp8_f32 v139, v61, v65 op_sel:[0,0,1]
	v_mul_f32_e32 v22, s30, v22
	v_mul_f32_e32 v26, s30, v26
	v_cvt_pk_fp8_f32 v140, v6, v10
	v_mul_f32_e32 v30, s30, v30
	v_mul_f32_e32 v34, s30, v34
	v_cvt_pk_fp8_f32 v140, v14, v18 op_sel:[0,0,1]
	v_mul_f32_e32 v38, s30, v38
	v_mul_f32_e32 v42, s30, v42
	v_cvt_pk_fp8_f32 v141, v22, v26
	v_mul_f32_e32 v46, s30, v46
	v_mul_f32_e32 v50, s30, v50
	v_cvt_pk_fp8_f32 v141, v30, v34 op_sel:[0,0,1]
	v_mul_f32_e32 v54, s30, v54
	v_mul_f32_e32 v58, s30, v58
	v_cvt_pk_fp8_f32 v142, v38, v42
	v_mul_f32_e32 v62, s30, v62
	v_mul_f32_e32 v66, s30, v66
	v_cvt_pk_fp8_f32 v142, v46, v50 op_sel:[0,0,1]
	v_mul_f32_e32 v7, s30, v7
	v_mul_f32_e32 v11, s30, v11
	v_cvt_pk_fp8_f32 v143, v54, v58
	v_mul_f32_e32 v15, s30, v15
	v_mul_f32_e32 v19, s30, v19
	v_cvt_pk_fp8_f32 v143, v62, v66 op_sel:[0,0,1]
	v_mul_f32_e32 v23, s30, v23
	v_mul_f32_e32 v27, s30, v27
	v_cvt_pk_fp8_f32 v144, v7, v11
	v_mul_f32_e32 v31, s30, v31
	v_mul_f32_e32 v35, s30, v35
	v_cvt_pk_fp8_f32 v144, v15, v19 op_sel:[0,0,1]
	v_mul_f32_e32 v39, s30, v39
	v_mul_f32_e32 v43, s30, v43
	v_cvt_pk_fp8_f32 v145, v23, v27
	v_mul_f32_e32 v47, s30, v47
	v_mul_f32_e32 v51, s30, v51
	v_cvt_pk_fp8_f32 v145, v31, v35 op_sel:[0,0,1]
	v_mul_f32_e32 v55, s30, v55
	v_mul_f32_e32 v59, s30, v59
	v_cvt_pk_fp8_f32 v146, v39, v43
	v_mul_f32_e32 v63, s30, v63
	v_mul_f32_e32 v67, s30, v67
	v_cvt_pk_fp8_f32 v146, v47, v51 op_sel:[0,0,1]
	v_cvt_pk_fp8_f32 v147, v55, v59
	s_add_u32 s11, s11, s7
	v_cvt_pk_fp8_f32 v147, v63, v67 op_sel:[0,0,1]
	s_nop 1
	v_permlane32_swap_b32_e32 v132, v140
	v_permlane32_swap_b32_e32 v133, v141
	v_permlane32_swap_b32_e32 v134, v142
	v_permlane32_swap_b32_e32 v135, v143
	v_permlane32_swap_b32_e32 v136, v144
	v_permlane32_swap_b32_e32 v137, v145
	v_permlane32_swap_b32_e32 v138, v146
	v_permlane32_swap_b32_e32 v139, v147
	v_permlane16_swap_b32_e32 v132, v136
	v_permlane16_swap_b32_e32 v133, v137
	v_permlane16_swap_b32_e32 v134, v138
	v_permlane16_swap_b32_e32 v135, v139
	v_permlane16_swap_b32_e32 v140, v144
	v_permlane16_swap_b32_e32 v141, v145
	v_permlane16_swap_b32_e32 v142, v146
	v_permlane16_swap_b32_e32 v143, v147
	global_store_dwordx4 v2, v[132:135], s[18:19]
	global_store_dwordx4 v2, v[136:139], s[18:19] offset:1024
	global_store_dwordx4 v2, v[140:143], s[18:19] offset:2048
	global_store_dwordx4 v2, v[144:147], s[18:19] offset:3072
	s_min_u32 s12, s10, s9
	s_lshr_b32 s13, s12, 15
	s_sub_u32 s13, 2, s13
	s_and_b32 s14, s12, 0x7fff
	s_lshr_b32 s15, s14, 3
	s_lshl_b32 s15, s15, 17
	s_and_b32 s14, s12, 7
	s_lshl_b32 s14, s14, 10
	s_or_b32 s15, s15, s14
	s_cmp_eq_u32 s13, 0
	s_cselect_b32 s16, s20, s22
	s_cselect_b32 s17, s21, s23
	s_cmp_eq_u32 s13, 2
	s_cselect_b32 s16, s24, s16
	s_cselect_b32 s17, s25, s17
	s_add_u32 s16, s16, s15
	s_addc_u32 s17, s17, 0
	global_load_dwordx4 v[4:7], v1, s[16:17] nt
	global_load_dwordx4 v[8:11], v148, s[16:17] nt
	global_load_dwordx4 v[12:15], v149, s[16:17] nt
	global_load_dwordx4 v[16:19], v150, s[16:17] nt
	global_load_dwordx4 v[20:23], v151, s[16:17] nt
	global_load_dwordx4 v[24:27], v152, s[16:17] nt
	global_load_dwordx4 v[28:31], v153, s[16:17] nt
	global_load_dwordx4 v[32:35], v154, s[16:17] nt
	global_load_dwordx4 v[36:39], v155, s[16:17] nt
	global_load_dwordx4 v[40:43], v156, s[16:17] nt
	global_load_dwordx4 v[44:47], v157, s[16:17] nt
	global_load_dwordx4 v[48:51], v158, s[16:17] nt
	global_load_dwordx4 v[52:55], v228, s[16:17] nt
	global_load_dwordx4 v[56:59], v229, s[16:17] nt
	global_load_dwordx4 v[60:63], v230, s[16:17] nt
	global_load_dwordx4 v[64:67], v231, s[16:17] nt
	s_add_u32 s10, s10, s7
; __device__ __forceinline__ unsigned pk_fp8x4(float a, float b, float c, float d) { int w = __builtin_amdgcn_cvt_pk_fp8_f32(a, b, 0, false); w = __builtin_amdgcn_cvt_pk_fp8_f32(c, d, w, true); return (unsigned)w; }
; __device__ __forceinline__ void convert_load(Frame& F, int it, f32x4 (&v)[16]) {
;     const int mat = it / TI_PER_MAT, r = it % TI_PER_MAT, type = mat / NE, e = mat % NE, kb = r >> 3, n4 = (r & 7) * 256 + F.lane * 4;
;     const float* src = F.in[type == 0 ? I_WGATE : (type == 1 ? I_WUP : I_WDOWN)] + (size_t)e * D * D + (size_t)(kb * 16) * D + n4;
; #pragma unroll
;     for (int i = 0; i < 16; ++i) v[i] = __builtin_nontemporal_load((const f32x4*)(src + (size_t)i * D));
; }
; __device__ __forceinline__ void convert_store(Frame& F, int it, const f32x4 (&v)[16]) {
;     const int mat = it / TI_PER_MAT, r = it % TI_PER_MAT, type = mat / NE, e = mat % NE, kb = r >> 3, n4 = (r & 7) * 256 + F.lane * 4;
;     unsigned char* dst = F.ws + (type == 0 ? WS_WG : (type == 1 ? WS_WU : WS_WD)) + (size_t)e * D * D + ((size_t)kb * D + n4) * 16;
; #pragma unroll
;     for (int nn = 0; nn < 4; ++nn)
;         *(u32x4*)(dst + nn * 16) = (u32x4){pk_fp8x4(v[0][nn] * W8_SCALE, v[1][nn] * W8_SCALE, v[2][nn] * W8_SCALE, v[3][nn] * W8_SCALE), pk_fp8x4(v[4][nn] * W8_SCALE, v[5][nn] * W8_SCALE, v[6][nn] * W8_SCALE, v[7][nn] * W8_SCALE),
;                                           pk_fp8x4(v[8][nn] * W8_SCALE, v[9][nn] * W8_SCALE, v[10][nn] * W8_SCALE, v[11][nn] * W8_SCALE), pk_fp8x4(v[12][nn] * W8_SCALE, v[13][nn] * W8_SCALE, v[14][nn] * W8_SCALE, v[15][nn] * W8_SCALE)};
; }
; __device__ __forceinline__ void convert_experts(Frame& F, int gw, int NGW, int it0, int it1) {
;     f32x4 A[16], B[16];
;     for (int it = it0 + gw; it < it1; it += 2 * NGW) {
;         const int i2 = it + NGW; const bool h2 = i2 < it1;
;         convert_load(F, it, A); convert_load(F, h2 ? i2 : it, B); __builtin_amdgcn_sched_barrier(0);
;         convert_store(F, it, A);
;         if (h2) convert_store(F, i2, B);
.Lcv2_l1:
	s_cmp_ge_u32 s11, s8
	s_cbranch_scc1 .Lcv2_done
	s_lshr_b32 s13, s11, 15
	s_sub_u32 s13, 2, s13
	s_and_b32 s14, s11, 0x7fff
	s_lshr_b32 s14, s14, 3
	s_lshl_b32 s14, s14, 15
	s_and_b32 s15, s11, 7
	s_lshl_b32 s15, s15, 12
	s_or_b32 s14, s14, s15
	s_lshl_b32 s13, s13, 28
	s_add_u32 s14, s14, s13
	s_add_u32 s18, s28, s14
	s_addc_u32 s19, s29, 0
	s_waitcnt vmcnt(40)
	v_mul_f32_e32 v68, s30, v68
	v_mul_f32_e32 v72, s30, v72
	v_mul_f32_e32 v76, s30, v76
	v_mul_f32_e32 v80, s30, v80
	v_mul_f32_e32 v84, s30, v84
	v_mul_f32_e32 v88, s30, v88
	v_cvt_pk_fp8_f32 v132, v68, v72
	v_mul_f32_e32 v92, s30, v92
	v_mul_f32_e32 v96, s30, v96
	v_cvt_pk_fp8_f32 v132, v76, v80 op_sel:[0,0,1]
	v_mul_f32_e32 v100, s30, v100
	v_mul_f32_e32 v104, s30, v104
	v_cvt_pk_fp8_f32 v133, v84, v88
	v_mul_f32_e32 v108, s30, v108
	v_mul_f32_e32 v112, s30, v112
	v_cvt_pk_fp8_f32 v133, v92, v96 op_sel:[0,0,1]
	v_mul_f32_e32 v116, s30, v116
	v_mul_f32_e32 v120, s30, v120
	v_cvt_pk_fp8_f32 v134, v100, v104
	v_mul_f32_e32 v124, s30, v124
	v_mul_f32_e32 v128, s30, v128
	v_cvt_pk_fp8_f32 v134, v108, v112 op_sel:[0,0,1]
	v_mul_f32_e32 v69, s30, v69
	v_mul_f32_e32 v73, s30, v73
	v_cvt_pk_fp8_f32 v135, v116, v120
	v_mul_f32_e32 v77, s30, v77
	v_mul_f32_e32 v81, s30, v81
	v_cvt_pk_fp8_f32 v135, v124, v128 op_sel:[0,0,1]
	v_mul_f32_e32 v85, s30, v85
	v_mul_f32_e32 v89, s30, v89
	v_cvt_pk_fp8_f32 v136, v69, v73
	v_mul_f32_e32 v93, s30, v93
	v_mul_f32_e32 v97, s30, v97
	v_cvt_pk_fp8_f32 v136, v77, v81 op_sel:[0,0,1]
	v_mul_f32_e32 v101, s30, v101
	v_mul_f32_e32 v105, s30, v105
	v_cvt_pk_fp8_f32 v137, v85, v89
	v_mul_f32_e32 v109, s30, v109
	v_mul_f32_e32 v113, s30, v113
	v_cvt_pk_fp8_f32 v137, v93, v97 op_sel:[0,0,1]
	v_mul_f32_e32 v117, s30, v117
	v_mul_f32_e32 v121, s30, v121
	v_cvt_pk_fp8_f32 v138, v101, v105
	v_mul_f32_e32 v125, s30, v125
	v_mul_f32_e32 v129, s30, v129
	v_cvt_pk_fp8_f32 v138, v109, v113 op_sel:[0,0,1]
	v_mul_f32_e32 v70, s30, v70
	v_mul_f32_e32 v74, s30, v74
	v_cvt_pk_fp8_f32 v139, v117, v121
	v_mul_f32_e32 v78, s30, v78
	v_mul_f32_e32 v82, s30, v82
	v_cvt_pk_fp8_f32 v139, v125, v129 op_sel:[0,0,1]
	v_mul_f32_e32 v86, s30, v86
	v_mul_f32_e32 v90, s30, v90
	v_cvt_pk_fp8_f32 v140, v70, v74
	v_mul_f32_e32 v94, s30, v94
	v_mul_f32_e32 v98, s30, v98
	v_cvt_pk_fp8_f32 v140, v78, v82 op_sel:[0,0,1]
	v_mul_f32_e32 v102, s30, v102
	v_mul_f32_e32 v106, s30, v106
	v_cvt_pk_fp8_f32 v141, v86, v90
	v_mul_f32_e32 v110, s30, v110
	v_mul_f32_e32 v114, s30, v114
	v_cvt_pk_fp8_f32 v141, v94, v98 op_sel:[0,0,1]
	v_mul_f32_e32 v118, s30, v118
	v_mul_f32_e32 v122, s30, v122
	v_cvt_pk_fp8_f32 v142, v102, v106
	v_mul_f32_e32 v126, s30, v126
	v_mul_f32_e32 v130, s30, v130
	v_cvt_pk_fp8_f32 v142, v110, v114 op_sel:[0,0,1]
	v_mul_f32_e32 v71, s30, v71
	v_mul_f32_e32 v75, s30, v75
	v_cvt_pk_fp8_f32 v143, v118, v122
	v_mul_f32_e32 v79, s30, v79
	v_mul_f32_e32 v83, s30, v83
	v_cvt_pk_fp8_f32 v143, v126, v130 op_sel:[0,0,1]
	v_mul_f32_e32 v87, s30, v87
	v_mul_f32_e32 v91, s30, v91
	v_cvt_pk_fp8_f32 v144, v71, v75
	v_mul_f32_e32 v95, s30, v95
	v_mul_f32_e32 v99, s30, v99
	v_cvt_pk_fp8_f32 v144, v79, v83 op_sel:[0,0,1]
	v_mul_f32_e32 v103, s30, v103
	v_mul_f32_e32 v107, s30, v107
	v_cvt_pk_fp8_f32 v145, v87, v91
	v_mul_f32_e32 v111, s30, v111
	v_mul_f32_e32 v115, s30, v115
	v_cvt_pk_fp8_f32 v145, v95, v99 op_sel:[0,0,1]
	v_mul_f32_e32 v119, s30, v119
	v_mul_f32_e32 v123, s30, v123
	v_cvt_pk_fp8_f32 v146, v103, v107
	v_mul_f32_e32 v127, s30, v127
	v_mul_f32_e32 v131, s30, v131
	v_cvt_pk_fp8_f32 v146, v111, v115 op_sel:[0,0,1]
	v_cvt_pk_fp8_f32 v147, v119, v123
	s_add_u32 s11, s11, s7
	v_cvt_pk_fp8_f32 v147, v127, v131 op_sel:[0,0,1]
	s_nop 1
	v_permlane32_swap_b32_e32 v132, v140
	v_permlane32_swap_b32_e32 v133, v141
	v_permlane32_swap_b32_e32 v134, v142
	v_permlane32_swap_b32_e32 v135, v143
	v_permlane32_swap_b32_e32 v136, v144
	v_permlane32_swap_b32_e32 v137, v145
	v_permlane32_swap_b32_e32 v138, v146
	v_permlane32_swap_b32_e32 v139, v147
	v_permlane16_swap_b32_e32 v132, v136
	v_permlane16_swap_b32_e32 v133, v137
	v_permlane16_swap_b32_e32 v134, v138
	v_permlane16_swap_b32_e32 v135, v139
	v_permlane16_swap_b32_e32 v140, v144
	v_permlane16_swap_b32_e32 v141, v145
	v_permlane16_swap_b32_e32 v142, v146
	v_permlane16_swap_b32_e32 v143, v147
	global_store_dwordx4 v2, v[132:135], s[18:19]
	global_store_dwordx4 v2, v[136:139], s[18:19] offset:1024
	global_store_dwordx4 v2, v[140:143], s[18:19] offset:2048
	global_store_dwordx4 v2, v[144:147], s[18:19] offset:3072
	s_min_u32 s12, s10, s9
	s_lshr_b32 s13, s12, 15
	s_sub_u32 s13, 2, s13
	s_and_b32 s14, s12, 0x7fff
	s_lshr_b32 s15, s14, 3
	s_lshl_b32 s15, s15, 17
	s_and_b32 s14, s12, 7
	s_lshl_b32 s14, s14, 10
	s_or_b32 s15, s15, s14
	s_cmp_eq_u32 s13, 0
	s_cselect_b32 s16, s20, s22
	s_cselect_b32 s17, s21, s23
	s_cmp_eq_u32 s13, 2
	s_cselect_b32 s16, s24, s16
	s_cselect_b32 s17, s25, s17
	s_add_u32 s16, s16, s15
	s_addc_u32 s17, s17, 0
	global_load_dwordx4 v[68:71], v1, s[16:17] nt
	global_load_dwordx4 v[72:75], v148, s[16:17] nt
	global_load_dwordx4 v[76:79], v149, s[16:17] nt
	global_load_dwordx4 v[80:83], v150, s[16:17] nt
	global_load_dwordx4 v[84:87], v151, s[16:17] nt
	global_load_dwordx4 v[88:91], v152, s[16:17] nt
	global_load_dwordx4 v[92:95], v153, s[16:17] nt
	global_load_dwordx4 v[96:99], v154, s[16:17] nt
	global_load_dwordx4 v[100:103], v155, s[16:17] nt
	global_load_dwordx4 v[104:107], v156, s[16:17] nt
	global_load_dwordx4 v[108:111], v157, s[16:17] nt
	global_load_dwordx4 v[112:115], v158, s[16:17] nt
	global_load_dwordx4 v[116:119], v228, s[16:17] nt
	global_load_dwordx4 v[120:123], v229, s[16:17] nt
	global_load_dwordx4 v[124:127], v230, s[16:17] nt
	global_load_dwordx4 v[128:131], v231, s[16:17] nt
	s_add_u32 s10, s10, s7
	s_branch .Lcv2_loop

; __device__ __forceinline__ unsigned pk_fp8x4(float a, float b, float c, float d) { int w = __builtin_amdgcn_cvt_pk_fp8_f32(a, b, 0, false); w = __builtin_amdgcn_cvt_pk_fp8_f32(c, d, w, true); return (unsigned)w; }
; __device__ __forceinline__ void convert_load(Frame& F, int it, f32x4 (&v)[16]) {
;     const int mat = it / TI_PER_MAT, r = it % TI_PER_MAT, type = mat / NE, e = mat % NE, kb = r >> 3, n4 = (r & 7) * 256 + F.lane * 4;
;     const float* src = F.in[type == 0 ? I_WGATE : (type == 1 ? I_WUP : I_WDOWN)] + (size_t)e * D * D + (size_t)(kb * 16) * D + n4;
; #pragma unroll
;     for (int i = 0; i < 16; ++i) v[i] = __builtin_nontemporal_load((const f32x4*)(src + (size_t)i * D));
; }
; __device__ __forceinline__ void convert_store(Frame& F, int it, const f32x4 (&v)[16]) {
;     const int mat = it / TI_PER_MAT, r = it % TI_PER_MAT, type = mat / NE, e = mat % NE, kb = r >> 3, n4 = (r & 7) * 256 + F.lane * 4;
;     unsigned char* dst = F.ws + (type == 0 ? WS_WG : (type == 1 ? WS_WU : WS_WD)) + (size_t)e * D * D + ((size_t)kb * D + n4) * 16;
; #pragma unroll
;     for (int nn = 0; nn < 4; ++nn)
;         *(u32x4*)(dst + nn * 16) = (u32x4){pk_fp8x4(v[0][nn] * W8_SCALE, v[1][nn] * W8_SCALE, v[2][nn] * W8_SCALE, v[3][nn] * W8_SCALE), pk_fp8x4(v[4][nn] * W8_SCALE, v[5][nn] * W8_SCALE, v[6][nn] * W8_SCALE, v[7][nn] * W8_SCALE),
;                                           pk_fp8x4(v[8][nn] * W8_SCALE, v[9][nn] * W8_SCALE, v[10][nn] * W8_SCALE, v[11][nn] * W8_SCALE), pk_fp8x4(v[12][nn] * W8_SCALE, v[13][nn] * W8_SCALE, v[14][nn] * W8_SCALE, v[15][nn] * W8_SCALE)};
; }
; __device__ __forceinline__ void convert_experts(Frame& F, int gw, int NGW, int it0, int it1) {
;     f32x4 A[16], B[16];
;     for (int it = it0 + gw; it < it1; it += 2 * NGW) {
;         const int i2 = it + NGW; const bool h2 = i2 < it1;
;         convert_load(F, it, A); convert_load(F, h2 ? i2 : it, B); __builtin_amdgcn_sched_barrier(0);
; __device__ __forceinline__ void p4_scan(Frame& F) {
;     constexpr int NSCAN = NBATCH * NH * 2;
;     if (F.bid >= NSCAN) {
;         const int nconv = (F.G - NSCAN) < NCONV_SCAN ? (F.G - NSCAN) : NCONV_SCAN;
;         if (F.bid - NSCAN < nconv) convert_experts(F, (F.bid - NSCAN) * 8 + F.wave, nconv * 8, ti_early(F.G), TI_EXP);
;         return;
.LBB0_721:
	s_and_b64 vcc, exec, s[0:1]
	s_cbranch_vccz .LBB0_728
	s_waitcnt lgkmcnt(0)
	s_min_i32 s0, s79, 0x90
	s_cmp_ge_i32 s80, s0
	s_cbranch_scc1 .LBB0_728
	s_lshl_b32 s1, s80, 3
	v_readlane_b32 s4, v253, 7
	s_add_i32 s4, s1, s4
	s_cmp_gt_i32 s79, 40
	s_cselect_b32 s7, 0x35c2, 0
	s_add_i32 s4, s4, s7
	s_addk_i32 s4, 0xff00
	s_cmp_gt_i32 s4, 0x17fff
	s_cbranch_scc1 .LBB0_728
	s_lshl_b32 s7, s0, 3
	s_addk_i32 s7, 0xff00
	s_mov_b32 s8, 0x18000
	s_load_dwordx2 s[20:21], s[88:89], 0x98
	s_load_dwordx2 s[22:23], s[88:89], 0xa8
	s_load_dwordx2 s[24:25], s[88:89], 0xb8
	s_add_u32 s28, s86, 0x3000000
	s_addc_u32 s29, s87, 0
	s_add_i32 s9, s8, -1
	s_mov_b32 s10, s4
	s_mov_b32 s11, s4
	s_mov_b32 s30, 0x42800000
	v_lshlrev_b32_e32 v1, 4, v162
	v_and_b32_e32 v2, 15, v162
	v_lshlrev_b32_e32 v2, 6, v2
	v_lshrrev_b32_e32 v3, 4, v162
	v_lshl_add_u32 v2, v3, 4, v2
	v_add_u32_e32 v148, 0x2000, v1
	v_add_u32_e32 v149, 0x4000, v1
	v_add_u32_e32 v150, 0x6000, v1
	v_add_u32_e32 v151, 0x8000, v1
	v_add_u32_e32 v152, 0xa000, v1
	v_add_u32_e32 v153, 0xc000, v1
	v_add_u32_e32 v154, 0xe000, v1
	v_add_u32_e32 v155, 0x10000, v1
	v_add_u32_e32 v156, 0x12000, v1
	v_add_u32_e32 v157, 0x14000, v1
	v_add_u32_e32 v158, 0x16000, v1
	v_add_u32_e32 v159, 0x18000, v1
	v_add_u32_e32 v160, 0x1a000, v1
	v_add_u32_e32 v161, 0x1c000, v1
	v_add_u32_e32 v163, 0x1e000, v1
	s_waitcnt lgkmcnt(0)
	s_min_u32 s12, s10, s9
	s_lshr_b32 s13, s12, 15
	s_sub_u32 s13, 2, s13
	s_and_b32 s14, s12, 0x7fff
	s_lshr_b32 s15, s14, 3
	s_lshl_b32 s15, s15, 17
	s_and_b32 s14, s12, 7
	s_lshl_b32 s14, s14, 10
	s_or_b32 s15, s15, s14
	s_cmp_eq_u32 s13, 0
	s_cselect_b32 s16, s20, s22
	s_cselect_b32 s17, s21, s23
	s_cmp_eq_u32 s13, 2
	s_cselect_b32 s16, s24, s16
	s_cselect_b32 s17, s25, s17
	s_add_u32 s16, s16, s15
	s_addc_u32 s17, s17, 0
	global_load_dwordx4 v[4:7], v1, s[16:17] nt
	global_load_dwordx4 v[8:11], v148, s[16:17] nt
	global_load_dwordx4 v[12:15], v149, s[16:17] nt
	global_load_dwordx4 v[16:19], v150, s[16:17] nt
	global_load_dwordx4 v[20:23], v151, s[16:17] nt
	global_load_dwordx4 v[24:27], v152, s[16:17] nt
	global_load_dwordx4 v[28:31], v153, s[16:17] nt
	global_load_dwordx4 v[32:35], v154, s[16:17] nt
	global_load_dwordx4 v[36:39], v155, s[16:17] nt
	global_load_dwordx4 v[40:43], v156, s[16:17] nt
	global_load_dwordx4 v[44:47], v157, s[16:17] nt
	global_load_dwordx4 v[48:51], v158, s[16:17] nt
	global_load_dwordx4 v[52:55], v159, s[16:17] nt
	global_load_dwordx4 v[56:59], v160, s[16:17] nt
	global_load_dwordx4 v[60:63], v161, s[16:17] nt
	global_load_dwordx4 v[64:67], v163, s[16:17] nt
	s_add_u32 s10, s10, s7
; __device__ __forceinline__ unsigned pk_fp8x4(float a, float b, float c, float d) { int w = __builtin_amdgcn_cvt_pk_fp8_f32(a, b, 0, false); w = __builtin_amdgcn_cvt_pk_fp8_f32(c, d, w, true); return (unsigned)w; }
; __device__ __forceinline__ void convert_load(Frame& F, int it, f32x4 (&v)[16]) {
;     const int mat = it / TI_PER_MAT, r = it % TI_PER_MAT, type = mat / NE, e = mat % NE, kb = r >> 3, n4 = (r & 7) * 256 + F.lane * 4;
;     const float* src = F.in[type == 0 ? I_WGATE : (type == 1 ? I_WUP : I_WDOWN)] + (size_t)e * D * D + (size_t)(kb * 16) * D + n4;
; #pragma unroll
;     for (int i = 0; i < 16; ++i) v[i] = __builtin_nontemporal_load((const f32x4*)(src + (size_t)i * D));
; }
; __device__ __forceinline__ void convert_store(Frame& F, int it, const f32x4 (&v)[16]) {
;     const int mat = it / TI_PER_MAT, r = it % TI_PER_MAT, type = mat / NE, e = mat % NE, kb = r >> 3, n4 = (r & 7) * 256 + F.lane * 4;
;     unsigned char* dst = F.ws + (type == 0 ? WS_WG : (type == 1 ? WS_WU : WS_WD)) + (size_t)e * D * D + ((size_t)kb * D + n4) * 16;
; #pragma unroll
;     for (int nn = 0; nn < 4; ++nn)
;         *(u32x4*)(dst + nn * 16) = (u32x4){pk_fp8x4(v[0][nn] * W8_SCALE, v[1][nn] * W8_SCALE, v[2][nn] * W8_SCALE, v[3][nn] * W8_SCALE), pk_fp8x4(v[4][nn] * W8_SCALE, v[5][nn] * W8_SCALE, v[6][nn] * W8_SCALE, v[7][nn] * W8_SCALE),
;                                           pk_fp8x4(v[8][nn] * W8_SCALE, v[9][nn] * W8_SCALE, v[10][nn] * W8_SCALE, v[11][nn] * W8_SCALE), pk_fp8x4(v[12][nn] * W8_SCALE, v[13][nn] * W8_SCALE, v[14][nn] * W8_SCALE, v[15][nn] * W8_SCALE)};
; }
; __device__ __forceinline__ void convert_experts(Frame& F, int gw, int NGW, int it0, int it1) {
;     f32x4 A[16], B[16];
;     for (int it = it0 + gw; it < it1; it += 2 * NGW) {
;         const int i2 = it + NGW; const bool h2 = i2 < it1;
;         convert_load(F, it, A); convert_load(F, h2 ? i2 : it, B); __builtin_amdgcn_sched_barrier(0);
;         convert_store(F, it, A);
;         if (h2) convert_store(F, i2, B);
.Lcv5_loop:
.Lcv5_l0:
	s_cmp_ge_u32 s11, s8
	s_cbranch_scc1 .Lcv5_done
	s_lshr_b32 s13, s11, 15
	s_sub_u32 s13, 2, s13
	s_and_b32 s14, s11, 0x7fff
	s_lshr_b32 s14, s14, 3
	s_lshl_b32 s14, s14, 15
	s_and_b32 s15, s11, 7
	s_lshl_b32 s15, s15, 12
	s_or_b32 s14, s14, s15
	s_lshl_b32 s13, s13, 28
	s_add_u32 s14, s14, s13
	s_add_u32 s18, s28, s14
	s_addc_u32 s19, s29, 0
	s_waitcnt vmcnt(0)
	v_mul_f32_e32 v4, s30, v4
	v_mul_f32_e32 v8, s30, v8
	v_mul_f32_e32 v12, s30, v12
	v_mul_f32_e32 v16, s30, v16
	v_mul_f32_e32 v20, s30, v20
	v_mul_f32_e32 v24, s30, v24
	v_cvt_pk_fp8_f32 v132, v4, v8
	v_mul_f32_e32 v28, s30, v28
	v_mul_f32_e32 v32, s30, v32
	v_cvt_pk_fp8_f32 v132, v12, v16 op_sel:[0,0,1]
	v_mul_f32_e32 v36, s30, v36
	v_mul_f32_e32 v40, s30, v40
	v_cvt_pk_fp8_f32 v133, v20, v24
	v_mul_f32_e32 v44, s30, v44
	v_mul_f32_e32 v48, s30, v48
	v_cvt_pk_fp8_f32 v133, v28, v32 op_sel:[0,0,1]
	v_mul_f32_e32 v52, s30, v52
	v_mul_f32_e32 v56, s30, v56
	v_cvt_pk_fp8_f32 v134, v36, v40
	v_mul_f32_e32 v60, s30, v60
	v_mul_f32_e32 v64, s30, v64
	v_cvt_pk_fp8_f32 v134, v44, v48 op_sel:[0,0,1]
	v_mul_f32_e32 v5, s30, v5
	v_mul_f32_e32 v9, s30, v9
	v_cvt_pk_fp8_f32 v135, v52, v56
	v_mul_f32_e32 v13, s30, v13
	v_mul_f32_e32 v17, s30, v17
	v_cvt_pk_fp8_f32 v135, v60, v64 op_sel:[0,0,1]
	v_mul_f32_e32 v21, s30, v21
	v_mul_f32_e32 v25, s30, v25
	v_cvt_pk_fp8_f32 v136, v5, v9
	v_mul_f32_e32 v29, s30, v29
	v_mul_f32_e32 v33, s30, v33
	v_cvt_pk_fp8_f32 v136, v13, v17 op_sel:[0,0,1]
	v_mul_f32_e32 v37, s30, v37
	v_mul_f32_e32 v41, s30, v41
	v_cvt_pk_fp8_f32 v137, v21, v25
	v_mul_f32_e32 v45, s30, v45
	v_mul_f32_e32 v49, s30, v49
	v_cvt_pk_fp8_f32 v137, v29, v33 op_sel:[0,0,1]
	v_mul_f32_e32 v53, s30, v53
	v_mul_f32_e32 v57, s30, v57
	v_cvt_pk_fp8_f32 v138, v37, v41
	v_mul_f32_e32 v61, s30, v61
	v_mul_f32_e32 v65, s30, v65
	v_cvt_pk_fp8_f32 v138, v45, v49 op_sel:[0,0,1]
	v_mul_f32_e32 v6, s30, v6
	v_mul_f32_e32 v10, s30, v10
	v_cvt_pk_fp8_f32 v139, v53, v57
	v_mul_f32_e32 v14, s30, v14
	v_mul_f32_e32 v18, s30, v18
	v_cvt_pk_fp8_f32 v139, v61, v65 op_sel:[0,0,1]
	v_mul_f32_e32 v22, s30, v22
	v_mul_f32_e32 v26, s30, v26
	v_cvt_pk_fp8_f32 v140, v6, v10
	v_mul_f32_e32 v30, s30, v30
	v_mul_f32_e32 v34, s30, v34
	v_cvt_pk_fp8_f32 v140, v14, v18 op_sel:[0,0,1]
	v_mul_f32_e32 v38, s30, v38
	v_mul_f32_e32 v42, s30, v42
	v_cvt_pk_fp8_f32 v141, v22, v26
	v_mul_f32_e32 v46, s30, v46
	v_mul_f32_e32 v50, s30, v50
	v_cvt_pk_fp8_f32 v141, v30, v34 op_sel:[0,0,1]
	v_mul_f32_e32 v54, s30, v54
	v_mul_f32_e32 v58, s30, v58
	v_cvt_pk_fp8_f32 v142, v38, v42
	v_mul_f32_e32 v62, s30, v62
	v_mul_f32_e32 v66, s30, v66
	v_cvt_pk_fp8_f32 v142, v46, v50 op_sel:[0,0,1]
	v_mul_f32_e32 v7, s30, v7
	v_mul_f32_e32 v11, s30, v11
	v_cvt_pk_fp8_f32 v143, v54, v58
	v_mul_f32_e32 v15, s30, v15
	v_mul_f32_e32 v19, s30, v19
	v_cvt_pk_fp8_f32 v143, v62, v66 op_sel:[0,0,1]
	v_mul_f32_e32 v23, s30, v23
	v_mul_f32_e32 v27, s30, v27
	v_cvt_pk_fp8_f32 v144, v7, v11
	v_mul_f32_e32 v31, s30, v31
	v_mul_f32_e32 v35, s30, v35
	v_cvt_pk_fp8_f32 v144, v15, v19 op_sel:[0,0,1]
	v_mul_f32_e32 v39, s30, v39
	v_mul_f32_e32 v43, s30, v43
	v_cvt_pk_fp8_f32 v145, v23, v27
	v_mul_f32_e32 v47, s30, v47
	v_mul_f32_e32 v51, s30, v51
	v_cvt_pk_fp8_f32 v145, v31, v35 op_sel:[0,0,1]
	v_mul_f32_e32 v55, s30, v55
	v_mul_f32_e32 v59, s30, v59
	v_cvt_pk_fp8_f32 v146, v39, v43
	v_mul_f32_e32 v63, s30, v63
	v_mul_f32_e32 v67, s30, v67
	v_cvt_pk_fp8_f32 v146, v47, v51 op_sel:[0,0,1]
	v_cvt_pk_fp8_f32 v147, v55, v59
	s_add_u32 s11, s11, s7
	v_cvt_pk_fp8_f32 v147, v63, v67 op_sel:[0,0,1]
	s_nop 1
	v_permlane32_swap_b32_e32 v132, v140
	v_permlane32_swap_b32_e32 v133, v141
	v_permlane32_swap_b32_e32 v134, v142
	v_permlane32_swap_b32_e32 v135, v143
	v_permlane32_swap_b32_e32 v136, v144
	v_permlane32_swap_b32_e32 v137, v145
	v_permlane32_swap_b32_e32 v138, v146
	v_permlane32_swap_b32_e32 v139, v147
	v_permlane16_swap_b32_e32 v132, v136
	v_permlane16_swap_b32_e32 v133, v137
	v_permlane16_swap_b32_e32 v134, v138
	v_permlane16_swap_b32_e32 v135, v139
	v_permlane16_swap_b32_e32 v140, v144
	v_permlane16_swap_b32_e32 v141, v145
	v_permlane16_swap_b32_e32 v142, v146
	v_permlane16_swap_b32_e32 v143, v147
	global_store_dwordx4 v2, v[132:135], s[18:19]
	global_store_dwordx4 v2, v[136:139], s[18:19] offset:1024
	global_store_dwordx4 v2, v[140:143], s[18:19] offset:2048
	global_store_dwordx4 v2, v[144:147], s[18:19] offset:3072
	s_min_u32 s12, s10, s9
	s_lshr_b32 s13, s12, 15
	s_sub_u32 s13, 2, s13
	s_and_b32 s14, s12, 0x7fff
	s_lshr_b32 s15, s14, 3
	s_lshl_b32 s15, s15, 17
	s_and_b32 s14, s12, 7
	s_lshl_b32 s14, s14, 10
	s_or_b32 s15, s15, s14
	s_cmp_eq_u32 s13, 0
	s_cselect_b32 s16, s20, s22
	s_cselect_b32 s17, s21, s23
	s_cmp_eq_u32 s13, 2
	s_cselect_b32 s16, s24, s16
	s_cselect_b32 s17, s25, s17
	s_add_u32 s16, s16, s15
	s_addc_u32 s17, s17, 0
	global_load_dwordx4 v[4:7], v1, s[16:17] nt
	global_load_dwordx4 v[8:11], v148, s[16:17] nt
	global_load_dwordx4 v[12:15], v149, s[16:17] nt
	global_load_dwordx4 v[16:19], v150, s[16:17] nt
	global_load_dwordx4 v[20:23], v151, s[16:17] nt
	global_load_dwordx4 v[24:27], v152, s[16:17] nt
	global_load_dwordx4 v[28:31], v153, s[16:17] nt
	global_load_dwordx4 v[32:35], v154, s[16:17] nt
	global_load_dwordx4 v[36:39], v155, s[16:17] nt
	global_load_dwordx4 v[40:43], v156, s[16:17] nt
	global_load_dwordx4 v[44:47], v157, s[16:17] nt
	global_load_dwordx4 v[48:51], v158, s[16:17] nt
	global_load_dwordx4 v[52:55], v159, s[16:17] nt
	global_load_dwordx4 v[56:59], v160, s[16:17] nt
	global_load_dwordx4 v[60:63], v161, s[16:17] nt
	global_load_dwordx4 v[64:67], v163, s[16:17] nt
	s_add_u32 s10, s10, s7
	s_branch .Lcv5_loop
